# v60 plus T5 bucket of the distance tables computed as trunc(log2(dist)*8/3+c) (bit-exact, as the reference's log formula) instead of a 15-step compare chain
# speedup vs baseline: 1.0226x; 1.0062x over previous
; __device__ __forceinline__ int t5_bucket(int n) {
;     if (n < 16) return n;
;     int b = 16;
;     b += (n >= 21); b += (n >= 27); b += (n >= 35); b += (n >= 46); b += (n >= 59); b += (n >= 77); b += (n >= 99); b += (n >= 128);
;     b += (n >= 166); b += (n >= 216); b += (n >= 280); b += (n >= 363); b += (n >= 470); b += (n >= 609); b += (n >= 790);
;     return b;
; }
;     ...
;                 for (int e = c.tid; e < 4 * NT; e += 512) { const int r = e / NT, dist = DOFF - (e - r * NT); const bool vis = dist >= 0 && (MODE != 0 || dist < 128) && (MODE != 1 || dist < 512);
;                     biasd[e] = vis ? reltab[t5_bucket(dist > 1023 ? 1023 : dist) * 16 + (MODE == 0 ? 8 : 0) + g * 4 + r] : -1e30f; } }
.LBB0_871:
	s_mov_b32 s6, 0x16f26017
	v_mul_hi_i32 v93, v92, s6
	v_lshrrev_b32_e32 v94, 31, v93
	v_ashrrev_i32_e32 v93, 8, v93
	v_add_u32_e32 v93, v93, v94
	s_movk_i32 s6, 0xf4d8
	v_mad_i32_i24 v94, v93, s6, v92
	s_movk_i32 s6, 0x720
	v_cmp_gt_i32_e32 vcc, s6, v94
	v_mov_b32_e32 v94, 0xf149f2ca
	s_and_saveexec_b64 s[28:29], vcc
	s_cbranch_execz .LBB0_870
	v_mul_i32_i24_e32 v94, 0xfffff4d8, v93
	v_sub_u32_e32 v94, v90, v94
	v_cmp_lt_u32_e32 vcc, 15, v94
	s_and_saveexec_b64 s[6:7], vcc
	s_cbranch_execz .LBB0_869
	v_cvt_f32_u32_e32 v95, v94
	v_log_f32_e32 v95, v95
	s_nop 0
	v_mul_f32_e32 v95, 0x402aaaab, v95
	v_add_f32_e32 v95, 0x40aaab7c, v95
	v_cvt_u32_f32_e32 v94, v95
	v_min_u32_e32 v94, 31, v94
	s_branch .LBB0_869

; __device__ __forceinline__ int t5_bucket(int n) {
;     if (n < 16) return n;
;     int b = 16;
;     b += (n >= 21); b += (n >= 27); b += (n >= 35); b += (n >= 46); b += (n >= 59); b += (n >= 77); b += (n >= 99); b += (n >= 128);
;     b += (n >= 166); b += (n >= 216); b += (n >= 280); b += (n >= 363); b += (n >= 470); b += (n >= 609); b += (n >= 790);
;     return b;
; }
;     ...
;                 for (int e = c.tid; e < 4 * NT; e += 512) { const int r = e / NT, dist = DOFF - (e - r * NT); const bool vis = dist >= 0 && (MODE != 0 || dist < 128) && (MODE != 1 || dist < 512);
;                     biasd[e] = vis ? reltab[t5_bucket(dist > 1023 ? 1023 : dist) * 16 + (MODE == 0 ? 8 : 0) + g * 4 + r] : -1e30f; } }
.LBB0_1007:
	v_mul_hi_i32 v21, v20, s31
	v_add_u32_e32 v21, v21, v20
	v_lshrrev_b32_e32 v22, 31, v21
	v_ashrrev_i32_e32 v21, 10, v21
	v_add_u32_e32 v21, v21, v22
	v_mad_i32_i24 v22, v21, s18, v20
	v_and_b32_e32 v23, 0xffffff80, v22
	v_cmp_eq_u32_e32 vcc, s19, v23
	v_mov_b32_e32 v23, 0xf149f2ca
	s_and_saveexec_b64 s[14:15], vcc
	s_cbranch_execz .LBB0_1006
	v_mul_i32_i24_e32 v23, 0xfffffb78, v21
	v_sub_u32_e32 v23, v18, v23
	v_cmp_gt_u32_e32 vcc, s34, v22
	s_and_saveexec_b64 s[16:17], vcc
	s_cbranch_execz .LBB0_1005
	v_cvt_f32_u32_e32 v24, v23
	v_log_f32_e32 v24, v24
	s_nop 0
	v_mul_f32_e32 v24, 0x402aaaab, v24
	v_add_f32_e32 v24, 0x40aaab7c, v24
	v_cvt_u32_f32_e32 v23, v24
	v_min_u32_e32 v23, 31, v23
	s_movk_i32 s46, 0x39d
	s_branch .LBB0_1005

; __device__ __forceinline__ int t5_bucket(int n) {
;     if (n < 16) return n;
;     int b = 16;
;     b += (n >= 21); b += (n >= 27); b += (n >= 35); b += (n >= 46); b += (n >= 59); b += (n >= 77); b += (n >= 99); b += (n >= 128);
;     b += (n >= 166); b += (n >= 216); b += (n >= 280); b += (n >= 363); b += (n >= 470); b += (n >= 609); b += (n >= 790);
;     return b;
; }
;     ...
;                 for (int e = c.tid; e < 4 * NT; e += 512) { const int r = e / NT, dist = DOFF - (e - r * NT); const bool vis = dist >= 0 && (MODE != 0 || dist < 128) && (MODE != 1 || dist < 512);
;                     biasd[e] = vis ? reltab[t5_bucket(dist > 1023 ? 1023 : dist) * 16 + (MODE == 0 ? 8 : 0) + g * 4 + r] : -1e30f; } }
.LBB0_1041:
	v_mul_hi_i32 v5, v4, s31
	v_add_u32_e32 v5, v5, v4
	v_lshrrev_b32_e32 v6, 31, v5
	v_ashrrev_i32_e32 v5, 10, v5
	v_add_u32_e32 v5, v5, v6
	v_mad_i32_i24 v6, v5, s18, v4
	v_and_b32_e32 v7, 0xfffffe00, v6
	s_movk_i32 s16, 0x200
	v_cmp_eq_u32_e32 vcc, s16, v7
	v_mov_b32_e32 v7, 0xf149f2ca
	s_and_saveexec_b64 s[16:17], vcc
	s_cbranch_execz .LBB0_1040
	v_mul_i32_i24_e32 v7, 0xfffffb78, v5
	v_sub_u32_e32 v7, v2, v7
	v_cmp_gt_u32_e32 vcc, s34, v6
	s_and_saveexec_b64 s[20:21], vcc
	s_cbranch_execz .LBB0_1039
	v_cvt_f32_u32_e32 v8, v7
	v_log_f32_e32 v8, v8
	s_nop 0
	v_mul_f32_e32 v8, 0x402aaaab, v8
	v_add_f32_e32 v8, 0x40aaab7c, v8
	v_cvt_u32_f32_e32 v7, v8
	v_min_u32_e32 v7, 31, v7
	s_movk_i32 s37, 0x22a
	s_branch .LBB0_1039

; __device__ __forceinline__ int t5_bucket(int n) {
;     if (n < 16) return n;
;     int b = 16;
;     b += (n >= 21); b += (n >= 27); b += (n >= 35); b += (n >= 46); b += (n >= 59); b += (n >= 77); b += (n >= 99); b += (n >= 128);
;     b += (n >= 166); b += (n >= 216); b += (n >= 280); b += (n >= 363); b += (n >= 470); b += (n >= 609); b += (n >= 790);
;     return b;
; }
;     ...
;                 for (int e = c.tid; e < 4 * NT; e += 512) { const int r = e / NT, dist = DOFF - (e - r * NT); const bool vis = dist >= 0 && (MODE != 0 || dist < 128) && (MODE != 1 || dist < 512);
;                     biasd[e] = vis ? reltab[t5_bucket(dist > 1023 ? 1023 : dist) * 16 + (MODE == 0 ? 8 : 0) + g * 4 + r] : -1e30f; } }
.LBB0_1146:
	v_mul_hi_i32 v77, v76, s31
	v_add_u32_e32 v77, v77, v76
	v_lshrrev_b32_e32 v78, 31, v77
	v_ashrrev_i32_e32 v77, 10, v77
	v_add_u32_e32 v77, v77, v78
	v_mad_i32_i24 v78, v77, s18, v76
	s_movk_i32 s14, 0x400
	v_cmp_gt_i32_e32 vcc, s14, v78
	v_mov_b32_e32 v78, 0xf149f2ca
	s_and_saveexec_b64 s[14:15], vcc
	s_cbranch_execz .LBB0_1145
	v_mul_i32_i24_e32 v78, 0xfffffb78, v77
	v_sub_u32_e32 v78, v74, v78
	v_cmp_lt_u32_e32 vcc, 15, v78
	s_and_saveexec_b64 s[16:17], vcc
	s_cbranch_execz .LBB0_1144
	v_cvt_f32_u32_e32 v79, v78
	v_log_f32_e32 v79, v79
	s_nop 0
	v_mul_f32_e32 v79, 0x402aaaab, v79
	v_add_f32_e32 v79, 0x40aaab7c, v79
	v_cvt_u32_f32_e32 v78, v79
	v_min_u32_e32 v78, 31, v78
	s_movk_i32 s42, 0x260
	s_branch .LBB0_1144
